# v30: prefetch the residual rows (x) of both out-proj tiles of each workgroup at the start of the out-proj phase (8 line-touch loads per wave into an unused VGPR), conv-phase pads kept
# baseline (speedup 1.0000x reference)
; #define LAS __attribute__((address_space(3)))
; #define VM_WAIT() asm volatile("s_waitcnt vmcnt(0)" ::: "memory")
;     __host__ __device__ bool next(int i, Unit& u) const {
;         const long L = (long)i * G + c; if (L >= nwg) return false;
;         int wgid = (int)L; { const int q = nwg / NXCD, r = nwg % NXCD, xcd = wgid % NXCD, off = wgid / NXCD; wgid = (xcd < r ? xcd * (q + 1) : r * (q + 1) + (xcd - r) * q) + off; }
;         const int nig = WGM * nN, gid = wgid / nig, fm = gid * WGM, gsz = (nM - fm) < WGM ? (nM - fm) : WGM;
;         u.pm = fm + ((wgid % nig) % gsz); u.pn = (wgid % nig) / gsz; return true;
; __global__ void __launch_bounds__(NWAVES * 64, 2) mega_fwd(Args args) {
;     ...
;     if (IN(7) && F.G == 256 && ((blockIdx.x >> 3) & 1)) { const int first = 256 * TR_UP_67 + (int)blockIdx.x * TR_UP_67; tr_run<6>(F, first + F.wave, first + TR_UP_67, NWAVES, (LAS float*)(F.lds + RING_OFF + F.wave * 16384)); VM_WAIT(); __syncthreads(); }
;     if (IN(7)) { pg8::Gemm g{F.MRG, F.WOUT, M, DM, DM, DM, DM}; pg8::StaticOrder S; S.init(M, DM, F.G, (int)blockIdx.x); EpiResid<false, true> E{F.x, F.MOD + 2 * DM, F.X1, 1.0f / (S_MRG * S_WOUT)};
.LBB0_1918:
	v_readlane_b32 s2, v249, 13
	v_readlane_b32 s3, v249, 14
	s_cmp_lt_i32 s2, 8
	s_cselect_b64 s[2:3], -1, 0
	s_and_b64 s[10:11], s[2:3], s[0:1]
	s_and_b64 s[14:15], s[10:11], s[4:5]
	s_and_b64 s[0:1], s[8:9], s[14:15]
	s_andn2_b64 vcc, exec, s[0:1]
	s_cbranch_vccnz .LBB0_2064
	v_readlane_b32 s60, v249, 38
	v_readlane_b32 s58, v249, 15
	v_readlane_b32 s59, v249, 16
	v_and_b32_e32 v2, 63, v0
	s_lshr_b32 s61, s60, 3
	s_and_b32 s62, s60, 7
	s_and_b32 s63, s61, 7
	s_lshr_b32 s64, s61, 3
	s_lshl_b32 s63, s63, 6
	s_add_i32 s63, s63, s64
	s_lshr_b32 s64, s63, 7
	s_and_b32 s65, s63, 0x7f
	s_and_b32 s66, s65, 7
	s_lshl_b32 s64, s64, 3
	s_add_i32 s64, s64, s66
	s_lshr_b32 s65, s65, 3
	s_lshl_b32 s62, s62, 6
	v_add_u32_e32 v2, s62, v2
	v_lshrrev_b32_e32 v3, 3, v2
	v_and_b32_e32 v2, 7, v2
	s_lshl_b32 s64, s64, 8
	v_add_u32_e32 v3, s64, v3
	v_lshlrev_b32_e32 v3, 14, v3
	v_lshlrev_b32_e32 v2, 7, v2
	s_lshl_b32 s65, s65, 10
	v_add3_u32 v2, v3, v2, s65
	s_add_u32 s66, s58, 0x1000
	s_addc_u32 s67, s59, 0
	global_load_dword v250, v2, s[58:59]
	global_load_dword v250, v2, s[66:67]
	s_add_u32 s58, s58, 0x100000
	s_addc_u32 s59, s59, 0
	s_add_u32 s66, s66, 0x100000
	s_addc_u32 s67, s67, 0
	global_load_dword v250, v2, s[58:59]
	global_load_dword v250, v2, s[66:67]
	s_add_u32 s58, s58, 0x100000
	s_addc_u32 s59, s59, 0
	s_add_u32 s66, s66, 0x100000
	s_addc_u32 s67, s67, 0
	global_load_dword v250, v2, s[58:59]
	global_load_dword v250, v2, s[66:67]
	s_add_u32 s58, s58, 0x100000
	s_addc_u32 s59, s59, 0
	s_add_u32 s66, s66, 0x100000
	s_addc_u32 s67, s67, 0
	global_load_dword v250, v2, s[58:59]
	global_load_dword v250, v2, s[66:67]
	v_readlane_b32 s0, v249, 36
	s_add_i32 s0, s56, s0
	s_add_i32 s41, s0, 0x2400
	s_add_i32 s33, s56, 0x2424
	s_cmp_lt_i32 s41, s33
	s_cselect_b64 s[24:25], -1, 0
	s_and_b64 vcc, exec, s[24:25]
	s_cbranch_vccnz .LBB0_1922
	v_lshrrev_b32_e32 v130, 3, v180
	v_lshlrev_b32_e32 v1, 2, v0
	v_and_b32_e32 v132, 28, v1
	v_mov_b32_e32 v133, 0
	v_or_b32_e32 v134, 64, v130
	s_cbranch_execz .LBB0_1923
	s_waitcnt vmcnt(0)
	v_mov_b32_e32 v2, 0
	v_mov_b32_e32 v3, v2
	v_mov_b32_e32 v4, v2
	v_mov_b32_e32 v5, v2
	v_mov_b32_e32 v6, v2
	v_mov_b32_e32 v7, v2
	v_mov_b32_e32 v8, v2
	v_mov_b32_e32 v9, v2
	v_mov_b32_e32 v10, v2
	v_mov_b32_e32 v11, v2
	v_mov_b32_e32 v12, v2
	v_mov_b32_e32 v13, v2
	v_mov_b32_e32 v14, v2
	v_mov_b32_e32 v15, v2
	v_mov_b32_e32 v16, v2
	v_mov_b32_e32 v17, v2
	v_mov_b32_e32 v18, v2
	v_mov_b32_e32 v19, v2
	v_mov_b32_e32 v20, v2
	v_mov_b32_e32 v21, v2
	v_mov_b32_e32 v22, v2
	v_mov_b32_e32 v23, v2
	v_mov_b32_e32 v24, v2
	v_mov_b32_e32 v25, v2
	v_mov_b32_e32 v26, v2
	v_mov_b32_e32 v27, v2
	v_mov_b32_e32 v28, v2
	v_mov_b32_e32 v29, v2
	v_mov_b32_e32 v30, v2
	v_mov_b32_e32 v31, v2
	v_mov_b32_e32 v32, v2
	v_mov_b32_e32 v33, v2
	s_branch .LBB0_1960

; __global__ void __launch_bounds__(NWAVES * 64, 2) mega_fwd(Args args) {
;     extern __shared__ __attribute__((aligned(16))) unsigned char lds[];
	.amdhsa_kernel _Z8mega_fwd4Args
		.amdhsa_group_segment_fixed_size 0
		.amdhsa_private_segment_fixed_size 0
		.amdhsa_kernarg_size 440
		.amdhsa_user_sgpr_count 2
		.amdhsa_user_sgpr_dispatch_ptr 0
		.amdhsa_user_sgpr_queue_ptr 0
		.amdhsa_user_sgpr_kernarg_segment_ptr 1
		.amdhsa_user_sgpr_dispatch_id 0
		.amdhsa_user_sgpr_kernarg_preload_length 0
		.amdhsa_user_sgpr_kernarg_preload_offset 0
		.amdhsa_user_sgpr_private_segment_size 0
		.amdhsa_uses_dynamic_stack 0
		.amdhsa_enable_private_segment 0
		.amdhsa_system_sgpr_workgroup_id_x 1
		.amdhsa_system_sgpr_workgroup_id_y 0
		.amdhsa_system_sgpr_workgroup_id_z 0
		.amdhsa_system_sgpr_workgroup_info 0
		.amdhsa_system_vgpr_workitem_id 0
		.amdhsa_next_free_vgpr 251
		.amdhsa_next_free_sgpr 98
		.amdhsa_accum_offset 252
		.amdhsa_reserve_vcc 1
		.amdhsa_float_round_mode_32 0
		.amdhsa_float_round_mode_16_64 0
		.amdhsa_float_denorm_mode_32 3
		.amdhsa_float_denorm_mode_16_64 3
		.amdhsa_dx10_clamp 1
		.amdhsa_ieee_mode 1
		.amdhsa_fp16_overflow 0
		.amdhsa_tg_split 0
		.amdhsa_exception_fp_ieee_invalid_op 0
		.amdhsa_exception_fp_denorm_src 0
		.amdhsa_exception_fp_ieee_div_zero 0
		.amdhsa_exception_fp_ieee_overflow 0
		.amdhsa_exception_fp_ieee_underflow 0
		.amdhsa_exception_fp_ieee_inexact 0
		.amdhsa_exception_int_div_zero 0
	.end_amdhsa_kernel

; __global__ void __launch_bounds__(NWAVES * 64, 2) mega_fwd(Args args) {
;     extern __shared__ __attribute__((aligned(16))) unsigned char lds[];
.Lfunc_end0:
	.size	_Z8mega_fwd4Args, .Lfunc_end0-_Z8mega_fwd4Args
	.set _Z8mega_fwd4Args.num_vgpr, 251
	.set _Z8mega_fwd4Args.num_agpr, 0
	.set _Z8mega_fwd4Args.numbered_sgpr, 98
	.set _Z8mega_fwd4Args.num_named_barrier, 0
	.set _Z8mega_fwd4Args.private_seg_size, 0
	.set _Z8mega_fwd4Args.uses_vcc, 1
	.set _Z8mega_fwd4Args.uses_flat_scratch, 0
	.set _Z8mega_fwd4Args.has_dyn_sized_stack, 0
	.set _Z8mega_fwd4Args.has_recursion, 0
	.set _Z8mega_fwd4Args.has_indirect_call, 0

; __global__ void __launch_bounds__(NWAVES * 64, 2) mega_fwd(Args args) {
;     extern __shared__ __attribute__((aligned(16))) unsigned char lds[];
amdhsa.kernels:
  - .agpr_count:     0
    .args:
      - .offset:         0
        .size:           184
        .value_kind:     by_value
      - .offset:         184
        .size:           4
        .value_kind:     hidden_block_count_x
      - .offset:         188
        .size:           4
        .value_kind:     hidden_block_count_y
      - .offset:         192
        .size:           4
        .value_kind:     hidden_block_count_z
      - .offset:         196
        .size:           2
        .value_kind:     hidden_group_size_x
      - .offset:         198
        .size:           2
        .value_kind:     hidden_group_size_y
      - .offset:         200
        .size:           2
        .value_kind:     hidden_group_size_z
      - .offset:         202
        .size:           2
        .value_kind:     hidden_remainder_x
      - .offset:         204
        .size:           2
        .value_kind:     hidden_remainder_y
      - .offset:         206
        .size:           2
        .value_kind:     hidden_remainder_z
      - .offset:         224
        .size:           8
        .value_kind:     hidden_global_offset_x
      - .offset:         232
        .size:           8
        .value_kind:     hidden_global_offset_y
      - .offset:         240
        .size:           8
        .value_kind:     hidden_global_offset_z
      - .offset:         248
        .size:           2
        .value_kind:     hidden_grid_dims
      - .offset:         304
        .size:           4
        .value_kind:     hidden_dynamic_lds_size
    .group_segment_fixed_size: 0
    .kernarg_segment_align: 8
    .kernarg_segment_size: 440
    .language:       OpenCL C
    .language_version:
      - 2
      - 0
    .max_flat_workgroup_size: 512
    .name:           _Z8mega_fwd4Args
    .private_segment_fixed_size: 0
    .sgpr_count:     104
    .sgpr_spill_count: 197
    .symbol:         _Z8mega_fwd4Args.kd
    .uniform_work_group_size: 1
    .uses_dynamic_stack: false
    .vgpr_count:     251
    .vgpr_spill_count: 0
    .wavefront_size: 64
